# GEMM unit start: first two DMA waits of a unit no longer force the previous epilogue's stores to drain (vmcnt(24)/(40) in the peeled first iteration, flagged strict after first/dt units)
# baseline (speedup 1.0000x reference)
.LBB0_256:
	s_or_b64 exec, exec, s[6:7]
	v_mov_b32_e32 v12, v0
	s_waitcnt lgkmcnt(0)
	s_barrier
	s_and_b64 vcc, exec, s[4:5]
	v_readfirstlane_b32 s5, v12
	s_cbranch_vccnz .LBB0_324
	s_mov_b32 s100, 0
	v_lshlrev_b32_e32 v1, 4, v12
	v_add_u32_e32 v2, 0x2000, v1
	v_ashrrev_i32_e32 v4, 31, v2
	v_lshrrev_b32_e32 v4, 22, v4
	v_add_u32_e32 v4, v2, v4
	v_ashrrev_i32_e32 v13, 10, v4
	v_mul_i32_i24_e32 v4, 0x400, v13
	v_sub_u32_e32 v2, v2, v4
	s_add_u32 s13, s36, s10
	v_lshrrev_b32_e32 v4, 4, v2
	s_addc_u32 s17, s37, s11
	s_ashr_i32 s16, s5, 6
	v_bitop3_b32 v2, v4, v2, 32 bitop3:0x6c
	s_ashr_i32 s4, s5, 8
	s_lshl_b32 s1, s16, 10
	v_readlane_b32 s6, v253, 29
	v_ashrrev_i32_e32 v4, 31, v2
	s_add_u32 s38, s13, 0x2b800000
	v_readlane_b32 s7, v253, 30
	s_mul_i32 s78, s6, 0x3500000
	v_lshrrev_b32_e32 v4, 26, v4
	s_addc_u32 s40, s17, 0
	s_lshl_b64 s[6:7], s[78:79], 1
	v_add_u32_e32 v4, v2, v4
	v_lshlrev_b32_e32 v5, 3, v13
	s_add_u32 s6, s13, s6
	v_ashrrev_i32_e32 v14, 6, v4
	v_and_b32_e32 v5, -16, v5
	s_addc_u32 s7, s17, s7
	v_add_u32_e32 v5, v14, v5
	s_add_u32 s42, s6, 0x1000000
	v_and_b32_e32 v6, 3, v14
	s_mov_b32 s6, 0x7ffe0
	v_lshrrev_b32_e32 v7, 2, v5
	v_lshlrev_b32_e32 v8, 1, v5
	v_and_b32_e32 v4, 0xc0, v4
	v_and_or_b32 v6, v5, s6, v6
	v_and_b32_e32 v7, 4, v7
	v_and_b32_e32 v8, 24, v8
	v_sub_u32_e32 v2, v2, v4
	v_or3_b32 v6, v6, v7, v8
	v_lshlrev_b32_e32 v7, 5, v13
	v_ashrrev_i16_sdwa v2, v208, sext(v2) dst_sel:DWORD dst_unused:UNUSED_PAD src0_sel:DWORD src1_sel:BYTE_0
	v_and_b32_e32 v7, 32, v7
	v_bfe_i32 v15, v2, 0, 16
	v_add_lshl_u32 v2, v7, v15, 1
	v_lshl_add_u32 v168, v6, 13, v2
	v_lshl_add_u32 v170, v5, 13, v2
	v_bfe_i32 v2, v12, 27, 1
	v_lshrrev_b32_e32 v2, 22, v2
	v_add_u32_e32 v2, v1, v2
	v_and_b32_e32 v2, 0xfffffc00, v2
	v_sub_u32_e32 v1, v1, v2
	v_lshrrev_b32_e32 v2, 4, v1
	v_ashrrev_i32_e32 v4, 31, v12
	v_bitop3_b32 v1, v2, v1, 32 bitop3:0x6c
	v_lshrrev_b32_e32 v4, 26, v4
	v_ashrrev_i32_e32 v2, 31, v1
	v_add_u32_e32 v4, v12, v4
	v_lshrrev_b32_e32 v2, 26, v2
	v_ashrrev_i32_e32 v17, 6, v4
	v_add_u32_e32 v2, v1, v2
	v_lshlrev_b32_e32 v4, 3, v17
	v_ashrrev_i32_e32 v16, 6, v2
	v_and_b32_e32 v4, -16, v4
	v_add_u32_e32 v4, v16, v4
	v_and_b32_e32 v5, 3, v16
	v_lshrrev_b32_e32 v6, 2, v4
	v_lshlrev_b32_e32 v7, 1, v4
	v_and_b32_e32 v2, 0xc0, v2
	v_and_or_b32 v5, v4, s6, v5
	v_and_b32_e32 v6, 4, v6
	v_and_b32_e32 v7, 24, v7
	v_sub_u32_e32 v1, v1, v2
	s_addc_u32 s44, s7, 0
	v_or3_b32 v5, v5, v6, v7
	v_lshlrev_b32_e32 v6, 5, v17
	v_ashrrev_i16_sdwa v1, v208, sext(v1) dst_sel:DWORD dst_unused:UNUSED_PAD src0_sel:DWORD src1_sel:BYTE_0
	v_readlane_b32 s6, v254, 29
	v_and_b32_e32 v6, 32, v6
	v_bfe_i32 v18, v1, 0, 16
	v_readlane_b32 s7, v254, 30
	s_add_u32 s24, s42, s6
	v_add_lshl_u32 v1, v6, v18, 1
	s_addc_u32 s25, s44, s7
	s_add_i32 s46, s1, 0
	v_lshl_add_u32 v2, v5, 13, v1
	s_add_i32 m0, s46, 0x10000
	v_lshl_add_u32 v172, v4, 13, v1
	global_load_lds_dwordx4 v2, s[24:25]
	s_add_i32 m0, s46, 0x12000
	s_add_u32 s6, s24, 0x100000
	global_load_lds_dwordx4 v168, s[24:25]
	s_addc_u32 s7, s25, 0
	s_add_i32 m0, s46, 0x14000
	v_mov_b32_e32 v169, v3
	global_load_lds_dwordx4 v2, s[6:7]
	s_add_i32 m0, s46, 0x16000
	v_mov_b32_e32 v173, v3
	global_load_lds_dwordx4 v168, s[6:7]
	v_readlane_b32 s6, v254, 27
	v_readlane_b32 s7, v254, 28
	s_add_u32 s6, s38, s6
	s_addc_u32 s7, s40, s7
	s_add_i32 s50, s46, 0x2000
	s_mov_b32 m0, s46
	s_add_u32 s8, s6, 0x100000
	global_load_lds_dwordx4 v172, s[6:7]
	s_mov_b32 m0, s50
	s_addc_u32 s9, s7, 0
	s_add_i32 s51, s46, 0x4000
	global_load_lds_dwordx4 v170, s[6:7]
	s_mov_b32 m0, s51
	s_add_i32 s54, s46, 0x6000
	global_load_lds_dwordx4 v172, s[8:9]
	s_mov_b32 m0, s54
	v_mov_b32_e32 v171, v3
	global_load_lds_dwordx4 v170, s[8:9]
	s_cmp_eq_u32 s4, 1
	v_lshl_add_u64 v[10:11], s[24:25], 0, v[2:3]
	v_lshl_add_u64 v[8:9], s[24:25], 0, v[168:169]
	v_lshl_add_u64 v[4:5], s[6:7], 0, v[172:173]
	s_cselect_b64 s[8:9], -1, 0
	s_cmp_lg_u32 s4, 1
	v_lshl_add_u64 v[6:7], s[6:7], 0, v[170:171]
	s_cbranch_scc1 .LBB0_259
	s_barrier

.LBB0_264:
	s_ashr_i32 s73, s72, 31
	s_lshl_b64 s[26:27], s[72:73], 21
	s_add_u32 s76, s38, s26
	s_addc_u32 s77, s40, s27
	s_and_b64 s[26:27], s[4:5], exec
	s_cselect_b32 s73, s77, s7
	s_cselect_b32 vcc_lo, s76, s6
	s_ashr_i32 s75, s74, 31
	s_lshl_b64 s[26:27], s[74:75], 21
	s_add_u32 s96, s42, s26
	s_addc_u32 s97, s44, s27
	s_and_b64 s[26:27], s[4:5], exec
	s_cselect_b32 s75, s97, s25
	s_cselect_b32 vcc_hi, s96, s24
	s_add_u32 s6, s6, 0x100080
	s_addc_u32 s7, s7, 0
	s_add_u32 s21, s24, 0x100
	s_addc_u32 s13, s25, 0
	s_mov_b32 s58, -2
	s_add_u32 s24, s6, 0xfff00080
	s_addc_u32 s25, s7, -1
	s_add_i32 s28, 0, 0x10000
	s_cmp_eq_u32 s58, 60
	s_cselect_b32 s27, s73, s25
	s_cselect_b32 s26, vcc_lo, s24
	s_cselect_b32 s25, s75, s13
	s_cselect_b32 s24, vcc_hi, s21
	s_add_i32 s71, 0, 0x14000
	v_add_u32_e32 v144, s28, v163
	v_add_u32_e32 v182, s71, v163
	s_waitcnt lgkmcnt(0)
	ds_read_b128 v[132:135], v144
	ds_read_b128 v[136:139], v144 offset:1024
	ds_read_b128 v[140:143], v144 offset:2048
	ds_read_b128 v[144:147], v144 offset:3072
	ds_read_b128 v[148:151], v182
	ds_read_b128 v[152:155], v182 offset:1024
	ds_read_b128 v[178:181], v182 offset:2048
	ds_read_b128 v[186:189], v182 offset:3072
	v_lshl_add_u64 v[182:183], s[6:7], 0, v[174:175]
	s_add_i32 m0, s46, 0xc000
	ds_read_b128 v[190:193], v184
	ds_read_b128 v[194:197], v184 offset:1024
	ds_read_b128 v[198:201], v184 offset:2048
	ds_read_b128 v[202:205], v184 offset:3072
	ds_read_b128 v[222:225], v184 offset:4096
	ds_read_b128 v[226:229], v184 offset:5120
	ds_read_b128 v[230:233], v184 offset:6144
	ds_read_b128 v[234:237], v184 offset:7168
	global_load_lds_dwordx4 v[182:183], off
	v_lshl_add_u64 v[182:183], s[6:7], 0, v[176:177]
	s_add_i32 m0, s46, 0xe000
	s_nop 0
	global_load_lds_dwordx4 v[182:183], off
	s_cmp_eq_u32 s100, 0
	s_cbranch_scc1 .Lrlx_i0_s
	s_waitcnt vmcnt(24)
	s_branch .Lrlx_i0_d
.Lrlx_i0_s:
	s_waitcnt vmcnt(8)
.Lrlx_i0_d:
	s_waitcnt lgkmcnt(0)
	s_setprio 1
	s_barrier
	v_mfma_f32_16x16x32_bf16 v[120:123], v[132:135], v[190:193], 0
	v_mfma_f32_16x16x32_bf16 v[116:119], v[140:143], v[190:193], 0
	v_mfma_f32_16x16x32_bf16 v[104:107], v[132:135], v[198:201], 0
	v_mfma_f32_16x16x32_bf16 v[100:103], v[140:143], v[198:201], 0
	v_mfma_f32_16x16x32_bf16 v[88:91], v[132:135], v[222:225], 0
	v_mfma_f32_16x16x32_bf16 v[84:87], v[140:143], v[222:225], 0
	v_mfma_f32_16x16x32_bf16 v[72:75], v[132:135], v[230:233], 0
	v_mfma_f32_16x16x32_bf16 v[68:71], v[140:143], v[230:233], 0
	v_mfma_f32_16x16x32_bf16 v[120:123], v[136:139], v[194:197], v[120:123]
	v_mfma_f32_16x16x32_bf16 v[116:119], v[144:147], v[194:197], v[116:119]
	v_mfma_f32_16x16x32_bf16 v[104:107], v[136:139], v[202:205], v[104:107]
	v_mfma_f32_16x16x32_bf16 v[100:103], v[144:147], v[202:205], v[100:103]
	v_mfma_f32_16x16x32_bf16 v[88:91], v[136:139], v[226:229], v[88:91]
	v_mfma_f32_16x16x32_bf16 v[84:87], v[144:147], v[226:229], v[84:87]
	v_mfma_f32_16x16x32_bf16 v[72:75], v[136:139], v[234:237], v[72:75]
	v_mfma_f32_16x16x32_bf16 v[68:71], v[144:147], v[234:237], v[68:71]
	v_mfma_f32_16x16x32_bf16 v[128:131], v[148:151], v[190:193], 0
	v_mfma_f32_16x16x32_bf16 v[124:127], v[178:181], v[190:193], 0
	v_mfma_f32_16x16x32_bf16 v[112:115], v[148:151], v[198:201], 0
	v_mfma_f32_16x16x32_bf16 v[108:111], v[178:181], v[198:201], 0
	v_mfma_f32_16x16x32_bf16 v[96:99], v[148:151], v[222:225], 0
	v_mfma_f32_16x16x32_bf16 v[92:95], v[178:181], v[222:225], 0
	v_mfma_f32_16x16x32_bf16 v[80:83], v[148:151], v[230:233], 0
	v_mfma_f32_16x16x32_bf16 v[76:79], v[178:181], v[230:233], 0
	v_mfma_f32_16x16x32_bf16 v[128:131], v[152:155], v[194:197], v[128:131]
	v_mfma_f32_16x16x32_bf16 v[124:127], v[186:189], v[194:197], v[124:127]
	v_mfma_f32_16x16x32_bf16 v[112:115], v[152:155], v[202:205], v[112:115]
	v_mfma_f32_16x16x32_bf16 v[108:111], v[186:189], v[202:205], v[108:111]
	v_mfma_f32_16x16x32_bf16 v[96:99], v[152:155], v[226:229], v[96:99]
	v_mfma_f32_16x16x32_bf16 v[92:95], v[186:189], v[226:229], v[92:95]
	v_mfma_f32_16x16x32_bf16 v[80:83], v[152:155], v[234:237], v[80:83]
	v_mfma_f32_16x16x32_bf16 v[76:79], v[186:189], v[234:237], v[76:79]
	s_barrier
	s_setprio 0
	s_add_i32 s28, s28, s1
	v_lshl_add_u64 v[182:183], s[24:25], 0, v[2:3]
	s_mov_b32 m0, s28
	ds_read_b128 v[190:193], v184 offset:16384
	ds_read_b128 v[194:197], v184 offset:17408
	ds_read_b128 v[198:201], v184 offset:18432
	ds_read_b128 v[202:205], v184 offset:19456
	ds_read_b128 v[222:225], v184 offset:20480
	ds_read_b128 v[226:229], v184 offset:21504
	ds_read_b128 v[230:233], v184 offset:22528
	ds_read_b128 v[234:237], v184 offset:23552
	global_load_lds_dwordx4 v[182:183], off
	s_add_i32 m0, s28, 0x2000
	s_add_u32 s28, s24, 0x100000
	v_lshl_add_u64 v[238:239], s[24:25], 0, v[168:169]
	s_addc_u32 s29, s25, 0
	s_add_i32 s71, s71, s1
	global_load_lds_dwordx4 v[238:239], off
	v_lshl_add_u64 v[240:241], s[28:29], 0, v[2:3]
	s_mov_b32 m0, s71
	v_lshl_add_u64 v[242:243], s[26:27], 0, v[170:171]
	global_load_lds_dwordx4 v[240:241], off
	v_lshl_add_u64 v[240:241], s[28:29], 0, v[168:169]
	s_add_i32 m0, s71, 0x2000
	s_nop 0
	global_load_lds_dwordx4 v[240:241], off
	v_lshl_add_u64 v[240:241], s[26:27], 0, v[172:173]
	s_mov_b32 m0, s46
	s_nop 0
	global_load_lds_dwordx4 v[240:241], off
	s_mov_b32 m0, s50
	s_nop 0
	global_load_lds_dwordx4 v[242:243], off
	s_cmp_eq_u32 s100, 0
	s_cbranch_scc1 .Lrlx_i1_s
	s_waitcnt vmcnt(24)
	s_branch .Lrlx_i1_d

.Lrlx_i1_d:
	s_waitcnt lgkmcnt(0)
	s_setprio 1
	s_barrier
	v_mfma_f32_16x16x32_bf16 v[56:59], v[132:135], v[190:193], 0
	v_mfma_f32_16x16x32_bf16 v[52:55], v[140:143], v[190:193], 0
	v_mfma_f32_16x16x32_bf16 v[40:43], v[132:135], v[198:201], 0
	v_mfma_f32_16x16x32_bf16 v[36:39], v[140:143], v[198:201], 0
	v_mfma_f32_16x16x32_bf16 v[24:27], v[132:135], v[222:225], 0
	v_mfma_f32_16x16x32_bf16 v[20:23], v[140:143], v[222:225], 0
	v_mfma_f32_16x16x32_bf16 v[8:11], v[132:135], v[230:233], 0
	v_mfma_f32_16x16x32_bf16 v[4:7], v[140:143], v[230:233], 0
	v_mfma_f32_16x16x32_bf16 v[56:59], v[136:139], v[194:197], v[56:59]
	v_mfma_f32_16x16x32_bf16 v[52:55], v[144:147], v[194:197], v[52:55]
	v_mfma_f32_16x16x32_bf16 v[40:43], v[136:139], v[202:205], v[40:43]
	v_mfma_f32_16x16x32_bf16 v[36:39], v[144:147], v[202:205], v[36:39]
	v_mfma_f32_16x16x32_bf16 v[24:27], v[136:139], v[226:229], v[24:27]
	v_mfma_f32_16x16x32_bf16 v[20:23], v[144:147], v[226:229], v[20:23]
	v_mfma_f32_16x16x32_bf16 v[8:11], v[136:139], v[234:237], v[8:11]
	v_mfma_f32_16x16x32_bf16 v[4:7], v[144:147], v[234:237], v[4:7]
	v_mfma_f32_16x16x32_bf16 v[64:67], v[148:151], v[190:193], 0
	v_mfma_f32_16x16x32_bf16 v[60:63], v[178:181], v[190:193], 0
	v_mfma_f32_16x16x32_bf16 v[48:51], v[148:151], v[198:201], 0
	v_mfma_f32_16x16x32_bf16 v[44:47], v[178:181], v[198:201], 0
	v_mfma_f32_16x16x32_bf16 v[32:35], v[148:151], v[222:225], 0
	v_mfma_f32_16x16x32_bf16 v[28:31], v[178:181], v[222:225], 0
	v_mfma_f32_16x16x32_bf16 v[16:19], v[148:151], v[230:233], 0
	v_mfma_f32_16x16x32_bf16 v[12:15], v[178:181], v[230:233], 0
	v_mfma_f32_16x16x32_bf16 v[64:67], v[152:155], v[194:197], v[64:67]
	v_mfma_f32_16x16x32_bf16 v[60:63], v[186:189], v[194:197], v[60:63]
	v_mfma_f32_16x16x32_bf16 v[48:51], v[152:155], v[202:205], v[48:51]
	v_mfma_f32_16x16x32_bf16 v[44:47], v[186:189], v[202:205], v[44:47]
	v_mfma_f32_16x16x32_bf16 v[32:35], v[152:155], v[226:229], v[32:35]
	v_mfma_f32_16x16x32_bf16 v[28:31], v[186:189], v[226:229], v[28:31]
	v_mfma_f32_16x16x32_bf16 v[16:19], v[152:155], v[234:237], v[16:19]
	v_mfma_f32_16x16x32_bf16 v[12:15], v[186:189], v[234:237], v[12:15]
	s_barrier
	s_setprio 0
	s_add_i32 s28, 0, 0x18000
	s_add_i32 s29, 0, 0x1c000
	v_add_u32_e32 v144, s28, v163
	v_add_u32_e32 v185, s29, v163
	ds_read_b128 v[132:135], v144
	ds_read_b128 v[136:139], v144 offset:1024
	ds_read_b128 v[140:143], v144 offset:2048
	ds_read_b128 v[144:147], v144 offset:3072
	ds_read_b128 v[148:151], v185
	ds_read_b128 v[152:155], v185 offset:1024
	ds_read_b128 v[178:181], v185 offset:2048
	ds_read_b128 v[186:189], v185 offset:3072
	s_add_u32 s26, s26, 0x100000
	s_addc_u32 s27, s27, 0
	s_mov_b32 m0, s51
	v_lshl_add_u64 v[244:245], s[26:27], 0, v[172:173]
	ds_read_b128 v[190:193], v184 offset:32768
	ds_read_b128 v[194:197], v184 offset:33792
	ds_read_b128 v[198:201], v184 offset:34816
	ds_read_b128 v[202:205], v184 offset:35840
	ds_read_b128 v[222:225], v184 offset:36864
	ds_read_b128 v[226:229], v184 offset:37888
	ds_read_b128 v[230:233], v184 offset:38912
	ds_read_b128 v[234:237], v184 offset:39936
	global_load_lds_dwordx4 v[244:245], off
	v_lshl_add_u64 v[244:245], s[26:27], 0, v[170:171]
	s_mov_b32 m0, s54
	s_nop 0
	global_load_lds_dwordx4 v[244:245], off
	s_waitcnt vmcnt(8)
	s_waitcnt lgkmcnt(0)
	s_setprio 1
	s_barrier
	v_mfma_f32_16x16x32_bf16 v[120:123], v[132:135], v[190:193], v[120:123]
	v_mfma_f32_16x16x32_bf16 v[116:119], v[140:143], v[190:193], v[116:119]
	v_mfma_f32_16x16x32_bf16 v[104:107], v[132:135], v[198:201], v[104:107]
	v_mfma_f32_16x16x32_bf16 v[100:103], v[140:143], v[198:201], v[100:103]
	v_mfma_f32_16x16x32_bf16 v[88:91], v[132:135], v[222:225], v[88:91]
	v_mfma_f32_16x16x32_bf16 v[84:87], v[140:143], v[222:225], v[84:87]
	v_mfma_f32_16x16x32_bf16 v[72:75], v[132:135], v[230:233], v[72:75]
	v_mfma_f32_16x16x32_bf16 v[68:71], v[140:143], v[230:233], v[68:71]
	v_mfma_f32_16x16x32_bf16 v[120:123], v[136:139], v[194:197], v[120:123]
	v_mfma_f32_16x16x32_bf16 v[116:119], v[144:147], v[194:197], v[116:119]
	v_mfma_f32_16x16x32_bf16 v[104:107], v[136:139], v[202:205], v[104:107]
	v_mfma_f32_16x16x32_bf16 v[100:103], v[144:147], v[202:205], v[100:103]
	v_mfma_f32_16x16x32_bf16 v[88:91], v[136:139], v[226:229], v[88:91]
	v_mfma_f32_16x16x32_bf16 v[84:87], v[144:147], v[226:229], v[84:87]
	v_mfma_f32_16x16x32_bf16 v[72:75], v[136:139], v[234:237], v[72:75]
	v_mfma_f32_16x16x32_bf16 v[68:71], v[144:147], v[234:237], v[68:71]
	v_mfma_f32_16x16x32_bf16 v[128:131], v[148:151], v[190:193], v[128:131]
	v_mfma_f32_16x16x32_bf16 v[124:127], v[178:181], v[190:193], v[124:127]
	v_mfma_f32_16x16x32_bf16 v[112:115], v[148:151], v[198:201], v[112:115]
	v_mfma_f32_16x16x32_bf16 v[108:111], v[178:181], v[198:201], v[108:111]
	v_mfma_f32_16x16x32_bf16 v[96:99], v[148:151], v[222:225], v[96:99]
	v_mfma_f32_16x16x32_bf16 v[92:95], v[178:181], v[222:225], v[92:95]
	v_mfma_f32_16x16x32_bf16 v[80:83], v[148:151], v[230:233], v[80:83]
	v_mfma_f32_16x16x32_bf16 v[76:79], v[178:181], v[230:233], v[76:79]
	v_mfma_f32_16x16x32_bf16 v[128:131], v[152:155], v[194:197], v[128:131]
	v_mfma_f32_16x16x32_bf16 v[124:127], v[186:189], v[194:197], v[124:127]
	v_mfma_f32_16x16x32_bf16 v[112:115], v[152:155], v[202:205], v[112:115]
	v_mfma_f32_16x16x32_bf16 v[108:111], v[186:189], v[202:205], v[108:111]
	v_mfma_f32_16x16x32_bf16 v[96:99], v[152:155], v[226:229], v[96:99]
	v_mfma_f32_16x16x32_bf16 v[92:95], v[186:189], v[226:229], v[92:95]
	v_mfma_f32_16x16x32_bf16 v[80:83], v[152:155], v[234:237], v[80:83]
	v_mfma_f32_16x16x32_bf16 v[76:79], v[186:189], v[234:237], v[76:79]
	s_barrier
	s_setprio 0
	s_add_i32 s26, s28, s1
	v_lshl_add_u64 v[182:183], v[182:183], 0, s[86:87]
	s_mov_b32 m0, s26
	ds_read_b128 v[190:193], v184 offset:49152
	ds_read_b128 v[194:197], v184 offset:50176
	ds_read_b128 v[198:201], v184 offset:51200
	ds_read_b128 v[202:205], v184 offset:52224
	ds_read_b128 v[222:225], v184 offset:53248
	ds_read_b128 v[226:229], v184 offset:54272
	ds_read_b128 v[230:233], v184 offset:55296
	ds_read_b128 v[234:237], v184 offset:56320
	global_load_lds_dwordx4 v[182:183], off
	s_add_i32 m0, s26, 0x2000
	s_add_u32 s24, s24, 0x100080
	v_lshl_add_u64 v[182:183], v[238:239], 0, s[86:87]
	s_addc_u32 s25, s25, 0
	s_add_i32 s26, s29, s1
	global_load_lds_dwordx4 v[182:183], off
	v_lshl_add_u64 v[182:183], s[24:25], 0, v[2:3]
	s_mov_b32 m0, s26
	s_nop 0
	global_load_lds_dwordx4 v[182:183], off
	v_lshl_add_u64 v[182:183], s[24:25], 0, v[168:169]
	s_add_i32 m0, s26, 0x2000
	s_nop 0
	global_load_lds_dwordx4 v[182:183], off
	v_lshl_add_u64 v[182:183], v[240:241], 0, s[86:87]
	s_mov_b32 m0, s78
	s_nop 0
	global_load_lds_dwordx4 v[182:183], off
	v_lshl_add_u64 v[182:183], v[242:243], 0, s[86:87]
	s_mov_b32 m0, s85
	s_nop 0
	global_load_lds_dwordx4 v[182:183], off
	s_waitcnt vmcnt(8)
	s_waitcnt lgkmcnt(0)
	s_setprio 1
	s_barrier
	v_mfma_f32_16x16x32_bf16 v[56:59], v[132:135], v[190:193], v[56:59]
	v_mfma_f32_16x16x32_bf16 v[52:55], v[140:143], v[190:193], v[52:55]
	v_mfma_f32_16x16x32_bf16 v[40:43], v[132:135], v[198:201], v[40:43]
	v_mfma_f32_16x16x32_bf16 v[36:39], v[140:143], v[198:201], v[36:39]
	v_mfma_f32_16x16x32_bf16 v[24:27], v[132:135], v[222:225], v[24:27]
	v_mfma_f32_16x16x32_bf16 v[20:23], v[140:143], v[222:225], v[20:23]
	v_mfma_f32_16x16x32_bf16 v[8:11], v[132:135], v[230:233], v[8:11]
	v_mfma_f32_16x16x32_bf16 v[4:7], v[140:143], v[230:233], v[4:7]
	v_mfma_f32_16x16x32_bf16 v[56:59], v[136:139], v[194:197], v[56:59]
	v_mfma_f32_16x16x32_bf16 v[52:55], v[144:147], v[194:197], v[52:55]
	v_mfma_f32_16x16x32_bf16 v[40:43], v[136:139], v[202:205], v[40:43]
	v_mfma_f32_16x16x32_bf16 v[36:39], v[144:147], v[202:205], v[36:39]
	v_mfma_f32_16x16x32_bf16 v[24:27], v[136:139], v[226:229], v[24:27]
	v_mfma_f32_16x16x32_bf16 v[20:23], v[144:147], v[226:229], v[20:23]
	v_mfma_f32_16x16x32_bf16 v[8:11], v[136:139], v[234:237], v[8:11]
	v_mfma_f32_16x16x32_bf16 v[4:7], v[144:147], v[234:237], v[4:7]
	v_mfma_f32_16x16x32_bf16 v[64:67], v[148:151], v[190:193], v[64:67]
	v_mfma_f32_16x16x32_bf16 v[60:63], v[178:181], v[190:193], v[60:63]
	v_mfma_f32_16x16x32_bf16 v[48:51], v[148:151], v[198:201], v[48:51]
	v_mfma_f32_16x16x32_bf16 v[44:47], v[178:181], v[198:201], v[44:47]
	v_mfma_f32_16x16x32_bf16 v[32:35], v[148:151], v[222:225], v[32:35]
	v_mfma_f32_16x16x32_bf16 v[28:31], v[178:181], v[222:225], v[28:31]
	v_mfma_f32_16x16x32_bf16 v[16:19], v[148:151], v[230:233], v[16:19]
	v_mfma_f32_16x16x32_bf16 v[12:15], v[178:181], v[230:233], v[12:15]
	v_mfma_f32_16x16x32_bf16 v[64:67], v[152:155], v[194:197], v[64:67]
	v_mfma_f32_16x16x32_bf16 v[60:63], v[186:189], v[194:197], v[60:63]
	v_mfma_f32_16x16x32_bf16 v[48:51], v[152:155], v[202:205], v[48:51]
	v_mfma_f32_16x16x32_bf16 v[44:47], v[186:189], v[202:205], v[44:47]
	v_mfma_f32_16x16x32_bf16 v[32:35], v[152:155], v[226:229], v[32:35]
	v_mfma_f32_16x16x32_bf16 v[28:31], v[186:189], v[226:229], v[28:31]
	v_mfma_f32_16x16x32_bf16 v[16:19], v[152:155], v[234:237], v[16:19]
	v_mfma_f32_16x16x32_bf16 v[12:15], v[186:189], v[234:237], v[12:15]
	s_barrier
	s_setprio 0
	s_add_i32 s58, s58, 2
	s_add_u32 s6, s6, 0x100
	s_addc_u32 s7, s7, 0
	s_add_u32 s21, s21, 0x100
	s_addc_u32 s13, s13, 0
	s_cmp_gt_u32 s58, 61
	s_cbranch_scc0 .LBB0_265

.LBB0_272:
	s_cmp_lt_i32 s92, 52
	s_cselect_b64 s[26:27], -1, 0
	s_cselect_b32 s100, 1, 0
	s_lshl_b32 s6, s92, 8
	s_or_b32 s6, s6, s61
	v_lshlrev_b32_e32 v134, 3, v185
	v_add_u32_e32 v136, s6, v134
	v_cmp_gt_i32_e32 vcc, 2, v185
	s_cmp_gt_i32 s92, 51
	v_ashrrev_i32_e32 v137, 31, v136
	s_mov_b64 s[6:7], -1
	s_cbranch_scc1 .LBB0_274
	v_mov_b64_e32 v[138:139], s[10:11]
	v_mad_i64_i32 v[138:139], s[6:7], v178, s3, v[138:139]
	s_waitcnt lgkmcnt(0)
	v_pk_mul_f32 v[142:143], v[120:121], v[180:181] op_sel_hi:[1,0]
	v_lshl_add_u64 v[138:139], v[136:137], 1, v[138:139]
	v_pk_mul_f32 v[144:145], v[122:123], v[180:181] op_sel_hi:[1,0]
	v_cvt_pk_bf16_f32 v142, v142, v143
	v_pk_mul_f32 v[146:147], v[118:119], v[180:181] op_sel_hi:[1,0]
	v_cvt_pk_bf16_f32 v143, v144, v145
	v_pk_mul_f32 v[150:151], v[116:117], v[180:181] op_sel_hi:[1,0]
	s_mov_b64 s[6:7], 0
	v_cvt_pk_bf16_f32 v144, v150, v151
	v_cvt_pk_bf16_f32 v145, v146, v147
	global_store_dwordx4 v[138:139], v[142:145], off
	v_pk_mul_f32 v[130:131], v[130:131], v[180:181] op_sel_hi:[1,0]
	v_pk_mul_f32 v[128:129], v[128:129], v[180:181] op_sel_hi:[1,0]
	v_pk_mul_f32 v[142:143], v[126:127], v[180:181] op_sel_hi:[1,0]
	v_pk_mul_f32 v[126:127], v[124:125], v[180:181] op_sel_hi:[1,0]
	v_cvt_pk_bf16_f32 v124, v128, v129
	v_cvt_pk_bf16_f32 v125, v130, v131
	s_nop 0
	v_cvt_pk_bf16_f32 v126, v126, v127
	v_cvt_pk_bf16_f32 v127, v142, v143
	global_store_dwordx4 v[138:139], v[124:127], off offset:256

.LBB0_1192:
	s_add_u32 s8, s10, 0x2b800000
	s_addc_u32 s9, s11, 0
	v_bfe_u32 v157, v18, 4, 2
	s_add_u32 s10, s10, 0x200000
	v_and_b32_e32 v1, 15, v18
	v_lshlrev_b32_e32 v19, 4, v157
	v_lshlrev_b32_e32 v18, 2, v18
	s_addc_u32 s11, s11, 0
	s_and_b32 s13, s13, 3
	s_lshl_b32 s55, s5, 6
	v_lshl_or_b32 v19, v1, 6, v19
	s_lshl_b32 s5, s5, 13
	v_and_b32_e32 v18, 32, v18
	s_add_i32 m0, s50, 0x18000
	v_lshl_add_u64 v[10:11], v[10:11], 0, s[86:87]
	v_bitop3_b32 v20, v19, s5, v18 bitop3:0xde
	s_lshl_b32 s61, s13, 5
	s_lshl_b32 s5, s13, 12
	global_load_lds_dwordx4 v[10:11], off
	v_lshl_add_u64 v[8:9], v[8:9], 0, s[86:87]
	s_add_i32 m0, s50, 0x1a000
	s_add_i32 s76, s50, 0x8000
	s_add_i32 s77, s50, 0xa000
	global_load_lds_dwordx4 v[8:9], off
	v_lshl_add_u64 v[4:5], v[4:5], 0, s[86:87]
	s_mov_b32 m0, s76
	s_add_u32 s14, s24, 0x100080
	global_load_lds_dwordx4 v[4:5], off
	v_lshl_add_u64 v[4:5], v[6:7], 0, s[86:87]
	s_mov_b32 m0, s77
	s_addc_u32 s15, s25, 0
	global_load_lds_dwordx4 v[4:5], off
	s_add_i32 m0, s50, 0x1c000
	v_lshl_add_u64 v[4:5], s[14:15], 0, v[2:3]
	global_load_lds_dwordx4 v[4:5], off
	v_lshl_add_u64 v[4:5], s[14:15], 0, v[132:133]
	s_add_i32 m0, s50, 0x1e000
	s_cmpk_lt_u32 s4, 0x100
	global_load_lds_dwordx4 v[4:5], off
	s_waitcnt vmcnt(8)
	s_barrier
	v_lshlrev_b32_e32 v4, 16, v15
	v_and_b32_e32 v4, 0xfffe0000, v4
	v_lshl_add_u32 v4, v16, 13, v4
	v_and_b32_e32 v5, 1, v15
	v_lshl_or_b32 v4, v5, 6, v4
	v_bitop3_b32 v163, v19, s5, v18 bitop3:0xde
	s_cselect_b64 s[14:15], -1, 0
	s_and_b32 s4, s4, 0xffffff00
	s_lshl_b32 s5, s13, 6
	v_lshl_add_u32 v134, v17, 1, v4
	v_lshlrev_b32_e32 v4, 16, v12
	s_or_b32 s78, s5, s4
	s_lshl_b32 s4, s13, 2
	v_and_b32_e32 v4, 0xfffe0000, v4
	s_waitcnt vmcnt(6)
	s_add_i32 s88, s4, 0
	v_lshl_add_u32 v4, v13, 13, v4
	v_and_b32_e32 v5, 1, v12
	v_readlane_b32 s4, v254, 24
	v_lshl_or_b32 v4, v5, 6, v4
	s_mov_b32 s16, s4
	v_readlane_b32 s4, v254, 31
	s_ashr_i32 s85, s22, 31
	s_add_i32 s88, s88, 0x20400
	v_mov_b32_e32 v135, v3
	v_lshl_add_u32 v136, v14, 1, v4
	v_mov_b32_e32 v137, v3
	s_mov_b32 s93, 0
	v_add_u32_e32 v186, 0, v20
	s_mov_b32 s17, s4
	s_barrier
	v_readlane_b32 s5, v254, 32
	s_mov_b32 s101, 0
	s_branch .LBB0_1195

.LBB0_1201:
	s_ashr_i32 s53, s52, 31
	s_lshl_b64 s[26:27], s[52:53], 21
	s_add_u32 s72, s38, s26
	s_addc_u32 s73, s40, s27
	s_and_b64 s[26:27], s[4:5], exec
	s_cselect_b32 s35, s73, s7
	s_cselect_b32 s53, s72, s6
	s_ashr_i32 s31, s30, 31
	s_lshl_b64 s[26:27], s[30:31], 21
	s_add_u32 s74, s42, s26
	s_addc_u32 s75, s44, s27
	s_and_b64 s[26:27], s[4:5], exec
	s_cselect_b32 s31, s75, s25
	s_cselect_b32 s92, s74, s24
	s_add_u32 s6, s6, 0x100080
	s_addc_u32 s7, s7, 0
	s_add_u32 s21, s24, 0x100
	s_addc_u32 s13, s25, 0
	s_mov_b32 s58, -2
	s_waitcnt lgkmcnt(0)
	s_add_u32 s24, s6, 0xfff00080
	s_addc_u32 s25, s7, -1
	s_add_i32 s28, 0, 0x10000
	s_cmp_eq_u32 s58, 60
	s_cselect_b32 s27, s35, s25
	s_cselect_b32 s26, s53, s24
	s_cselect_b32 s25, s31, s13
	s_cselect_b32 s24, s92, s21
	s_add_i32 s71, 0, 0x14000
	v_add_u32_e32 v150, s28, v163
	v_add_u32_e32 v154, s71, v163
	ds_read_b128 v[138:141], v150
	ds_read_b128 v[142:145], v150 offset:1024
	ds_read_b128 v[146:149], v150 offset:2048
	ds_read_b128 v[150:153], v150 offset:3072
	ds_read_b128 v[168:171], v154
	ds_read_b128 v[172:175], v154 offset:1024
	ds_read_b128 v[176:179], v154 offset:2048
	ds_read_b128 v[180:183], v154 offset:3072
	v_lshl_add_u64 v[154:155], s[6:7], 0, v[134:135]
	s_add_i32 m0, s50, 0xc000
	ds_read_b128 v[188:191], v186
	ds_read_b128 v[192:195], v186 offset:1024
	ds_read_b128 v[196:199], v186 offset:2048
	ds_read_b128 v[200:203], v186 offset:3072
	ds_read_b128 v[222:225], v186 offset:4096
	ds_read_b128 v[226:229], v186 offset:5120
	ds_read_b128 v[230:233], v186 offset:6144
	ds_read_b128 v[234:237], v186 offset:7168
	global_load_lds_dwordx4 v[154:155], off
	v_lshl_add_u64 v[154:155], s[6:7], 0, v[136:137]
	s_add_i32 m0, s50, 0xe000
	s_nop 0
	global_load_lds_dwordx4 v[154:155], off
	s_cmp_eq_u32 s101, 0
	s_cbranch_scc1 .Lrlx_o0_s
	s_waitcnt vmcnt(40)
	s_branch .Lrlx_o0_d

.Lrlx_o0_d:
	s_waitcnt lgkmcnt(0)
	s_setprio 1
	s_barrier
	v_mfma_f32_16x16x32_bf16 v[128:131], v[138:141], v[188:191], 0
	v_mfma_f32_16x16x32_bf16 v[124:127], v[146:149], v[188:191], 0
	v_mfma_f32_16x16x32_bf16 v[112:115], v[138:141], v[196:199], 0
	v_mfma_f32_16x16x32_bf16 v[108:111], v[146:149], v[196:199], 0
	v_mfma_f32_16x16x32_bf16 v[96:99], v[138:141], v[222:225], 0
	v_mfma_f32_16x16x32_bf16 v[92:95], v[146:149], v[222:225], 0
	v_mfma_f32_16x16x32_bf16 v[80:83], v[138:141], v[230:233], 0
	v_mfma_f32_16x16x32_bf16 v[76:79], v[146:149], v[230:233], 0
	v_mfma_f32_16x16x32_bf16 v[128:131], v[142:145], v[192:195], v[128:131]
	v_mfma_f32_16x16x32_bf16 v[124:127], v[150:153], v[192:195], v[124:127]
	v_mfma_f32_16x16x32_bf16 v[112:115], v[142:145], v[200:203], v[112:115]
	v_mfma_f32_16x16x32_bf16 v[108:111], v[150:153], v[200:203], v[108:111]
	v_mfma_f32_16x16x32_bf16 v[96:99], v[142:145], v[226:229], v[96:99]
	v_mfma_f32_16x16x32_bf16 v[92:95], v[150:153], v[226:229], v[92:95]
	v_mfma_f32_16x16x32_bf16 v[80:83], v[142:145], v[234:237], v[80:83]
	v_mfma_f32_16x16x32_bf16 v[76:79], v[150:153], v[234:237], v[76:79]
	v_mfma_f32_16x16x32_bf16 v[120:123], v[168:171], v[188:191], 0
	v_mfma_f32_16x16x32_bf16 v[116:119], v[176:179], v[188:191], 0
	v_mfma_f32_16x16x32_bf16 v[104:107], v[168:171], v[196:199], 0
	v_mfma_f32_16x16x32_bf16 v[100:103], v[176:179], v[196:199], 0
	v_mfma_f32_16x16x32_bf16 v[88:91], v[168:171], v[222:225], 0
	v_mfma_f32_16x16x32_bf16 v[84:87], v[176:179], v[222:225], 0
	v_mfma_f32_16x16x32_bf16 v[72:75], v[168:171], v[230:233], 0
	v_mfma_f32_16x16x32_bf16 v[68:71], v[176:179], v[230:233], 0
	v_mfma_f32_16x16x32_bf16 v[120:123], v[172:175], v[192:195], v[120:123]
	v_mfma_f32_16x16x32_bf16 v[116:119], v[180:183], v[192:195], v[116:119]
	v_mfma_f32_16x16x32_bf16 v[104:107], v[172:175], v[200:203], v[104:107]
	v_mfma_f32_16x16x32_bf16 v[100:103], v[180:183], v[200:203], v[100:103]
	v_mfma_f32_16x16x32_bf16 v[88:91], v[172:175], v[226:229], v[88:91]
	v_mfma_f32_16x16x32_bf16 v[84:87], v[180:183], v[226:229], v[84:87]
	v_mfma_f32_16x16x32_bf16 v[72:75], v[172:175], v[234:237], v[72:75]
	v_mfma_f32_16x16x32_bf16 v[68:71], v[180:183], v[234:237], v[68:71]
	s_barrier
	s_setprio 0
	s_add_i32 s28, s28, s46
	v_lshl_add_u64 v[154:155], s[24:25], 0, v[2:3]
	s_mov_b32 m0, s28
	ds_read_b128 v[188:191], v186 offset:16384
	ds_read_b128 v[192:195], v186 offset:17408
	ds_read_b128 v[196:199], v186 offset:18432
	ds_read_b128 v[200:203], v186 offset:19456
	ds_read_b128 v[222:225], v186 offset:20480
	ds_read_b128 v[226:229], v186 offset:21504
	ds_read_b128 v[230:233], v186 offset:22528
	ds_read_b128 v[234:237], v186 offset:23552
	global_load_lds_dwordx4 v[154:155], off
	s_add_i32 m0, s28, 0x2000
	s_add_u32 s28, s24, 0x100000
	v_lshl_add_u64 v[184:185], s[24:25], 0, v[132:133]
	s_addc_u32 s29, s25, 0
	s_add_i32 s71, s71, s46
	global_load_lds_dwordx4 v[184:185], off
	v_lshl_add_u64 v[204:205], s[28:29], 0, v[2:3]
	s_mov_b32 m0, s71
	v_lshl_add_u64 v[238:239], s[26:27], 0, v[132:133]
	global_load_lds_dwordx4 v[204:205], off
	v_lshl_add_u64 v[204:205], s[28:29], 0, v[132:133]
	s_add_i32 m0, s71, 0x2000
	s_nop 0
	global_load_lds_dwordx4 v[204:205], off
	v_lshl_add_u64 v[204:205], s[26:27], 0, v[2:3]
	s_mov_b32 m0, s50
	s_nop 0
	global_load_lds_dwordx4 v[204:205], off
	s_mov_b32 m0, s23
	s_nop 0
	global_load_lds_dwordx4 v[238:239], off
	s_cmp_eq_u32 s101, 0
	s_cbranch_scc1 .Lrlx_o1_s
	s_waitcnt vmcnt(40)
	s_branch .Lrlx_o1_d

.Lrlx_o1_d:
	s_waitcnt lgkmcnt(0)
	s_setprio 1
	s_barrier
	v_mfma_f32_16x16x32_bf16 v[64:67], v[138:141], v[188:191], 0
	v_mfma_f32_16x16x32_bf16 v[60:63], v[146:149], v[188:191], 0
	v_mfma_f32_16x16x32_bf16 v[48:51], v[138:141], v[196:199], 0
	v_mfma_f32_16x16x32_bf16 v[44:47], v[146:149], v[196:199], 0
	v_mfma_f32_16x16x32_bf16 v[32:35], v[138:141], v[222:225], 0
	v_mfma_f32_16x16x32_bf16 v[28:31], v[146:149], v[222:225], 0
	v_mfma_f32_16x16x32_bf16 v[16:19], v[138:141], v[230:233], 0
	v_mfma_f32_16x16x32_bf16 v[12:15], v[146:149], v[230:233], 0
	v_mfma_f32_16x16x32_bf16 v[64:67], v[142:145], v[192:195], v[64:67]
	v_mfma_f32_16x16x32_bf16 v[60:63], v[150:153], v[192:195], v[60:63]
	v_mfma_f32_16x16x32_bf16 v[48:51], v[142:145], v[200:203], v[48:51]
	v_mfma_f32_16x16x32_bf16 v[44:47], v[150:153], v[200:203], v[44:47]
	v_mfma_f32_16x16x32_bf16 v[32:35], v[142:145], v[226:229], v[32:35]
	v_mfma_f32_16x16x32_bf16 v[28:31], v[150:153], v[226:229], v[28:31]
	v_mfma_f32_16x16x32_bf16 v[16:19], v[142:145], v[234:237], v[16:19]
	v_mfma_f32_16x16x32_bf16 v[12:15], v[150:153], v[234:237], v[12:15]
	v_mfma_f32_16x16x32_bf16 v[56:59], v[168:171], v[188:191], 0
	v_mfma_f32_16x16x32_bf16 v[52:55], v[176:179], v[188:191], 0
	v_mfma_f32_16x16x32_bf16 v[40:43], v[168:171], v[196:199], 0
	v_mfma_f32_16x16x32_bf16 v[36:39], v[176:179], v[196:199], 0
	v_mfma_f32_16x16x32_bf16 v[24:27], v[168:171], v[222:225], 0
	v_mfma_f32_16x16x32_bf16 v[20:23], v[176:179], v[222:225], 0
	v_mfma_f32_16x16x32_bf16 v[8:11], v[168:171], v[230:233], 0
	v_mfma_f32_16x16x32_bf16 v[4:7], v[176:179], v[230:233], 0
	v_mfma_f32_16x16x32_bf16 v[56:59], v[172:175], v[192:195], v[56:59]
	v_mfma_f32_16x16x32_bf16 v[52:55], v[180:183], v[192:195], v[52:55]
	v_mfma_f32_16x16x32_bf16 v[40:43], v[172:175], v[200:203], v[40:43]
	v_mfma_f32_16x16x32_bf16 v[36:39], v[180:183], v[200:203], v[36:39]
	v_mfma_f32_16x16x32_bf16 v[24:27], v[172:175], v[226:229], v[24:27]
	v_mfma_f32_16x16x32_bf16 v[20:23], v[180:183], v[226:229], v[20:23]
	v_mfma_f32_16x16x32_bf16 v[8:11], v[172:175], v[234:237], v[8:11]
	v_mfma_f32_16x16x32_bf16 v[4:7], v[180:183], v[234:237], v[4:7]
	s_barrier
	s_setprio 0
	s_add_i32 s28, 0, 0x18000
	s_add_i32 s29, 0, 0x1c000
	v_add_u32_e32 v150, s28, v163
	v_add_u32_e32 v180, s29, v163
	ds_read_b128 v[138:141], v150
	ds_read_b128 v[142:145], v150 offset:1024
	ds_read_b128 v[146:149], v150 offset:2048
	ds_read_b128 v[150:153], v150 offset:3072
	ds_read_b128 v[168:171], v180
	ds_read_b128 v[172:175], v180 offset:1024
	ds_read_b128 v[176:179], v180 offset:2048
	ds_read_b128 v[180:183], v180 offset:3072
	s_add_u32 s26, s26, 0x100000
	s_addc_u32 s27, s27, 0
	s_mov_b32 m0, s51
	v_lshl_add_u64 v[240:241], s[26:27], 0, v[2:3]
	ds_read_b128 v[188:191], v186 offset:32768
	ds_read_b128 v[192:195], v186 offset:33792
	ds_read_b128 v[196:199], v186 offset:34816
	ds_read_b128 v[200:203], v186 offset:35840
	ds_read_b128 v[222:225], v186 offset:36864
	ds_read_b128 v[226:229], v186 offset:37888
	ds_read_b128 v[230:233], v186 offset:38912
	ds_read_b128 v[234:237], v186 offset:39936
	global_load_lds_dwordx4 v[240:241], off
	v_lshl_add_u64 v[240:241], s[26:27], 0, v[132:133]
	s_mov_b32 m0, s54
	s_nop 0
	global_load_lds_dwordx4 v[240:241], off
	s_waitcnt vmcnt(8)
	s_waitcnt lgkmcnt(0)
	s_setprio 1
	s_barrier
	v_mfma_f32_16x16x32_bf16 v[128:131], v[138:141], v[188:191], v[128:131]
	v_mfma_f32_16x16x32_bf16 v[124:127], v[146:149], v[188:191], v[124:127]
	v_mfma_f32_16x16x32_bf16 v[112:115], v[138:141], v[196:199], v[112:115]
	v_mfma_f32_16x16x32_bf16 v[108:111], v[146:149], v[196:199], v[108:111]
	v_mfma_f32_16x16x32_bf16 v[96:99], v[138:141], v[222:225], v[96:99]
	v_mfma_f32_16x16x32_bf16 v[92:95], v[146:149], v[222:225], v[92:95]
	v_mfma_f32_16x16x32_bf16 v[80:83], v[138:141], v[230:233], v[80:83]
	v_mfma_f32_16x16x32_bf16 v[76:79], v[146:149], v[230:233], v[76:79]
	v_mfma_f32_16x16x32_bf16 v[128:131], v[142:145], v[192:195], v[128:131]
	v_mfma_f32_16x16x32_bf16 v[124:127], v[150:153], v[192:195], v[124:127]
	v_mfma_f32_16x16x32_bf16 v[112:115], v[142:145], v[200:203], v[112:115]
	v_mfma_f32_16x16x32_bf16 v[108:111], v[150:153], v[200:203], v[108:111]
	v_mfma_f32_16x16x32_bf16 v[96:99], v[142:145], v[226:229], v[96:99]
	v_mfma_f32_16x16x32_bf16 v[92:95], v[150:153], v[226:229], v[92:95]
	v_mfma_f32_16x16x32_bf16 v[80:83], v[142:145], v[234:237], v[80:83]
	v_mfma_f32_16x16x32_bf16 v[76:79], v[150:153], v[234:237], v[76:79]
	v_mfma_f32_16x16x32_bf16 v[120:123], v[168:171], v[188:191], v[120:123]
	v_mfma_f32_16x16x32_bf16 v[116:119], v[176:179], v[188:191], v[116:119]
	v_mfma_f32_16x16x32_bf16 v[104:107], v[168:171], v[196:199], v[104:107]
	v_mfma_f32_16x16x32_bf16 v[100:103], v[176:179], v[196:199], v[100:103]
	v_mfma_f32_16x16x32_bf16 v[88:91], v[168:171], v[222:225], v[88:91]
	v_mfma_f32_16x16x32_bf16 v[84:87], v[176:179], v[222:225], v[84:87]
	v_mfma_f32_16x16x32_bf16 v[72:75], v[168:171], v[230:233], v[72:75]
	v_mfma_f32_16x16x32_bf16 v[68:71], v[176:179], v[230:233], v[68:71]
	v_mfma_f32_16x16x32_bf16 v[120:123], v[172:175], v[192:195], v[120:123]
	v_mfma_f32_16x16x32_bf16 v[116:119], v[180:183], v[192:195], v[116:119]
	v_mfma_f32_16x16x32_bf16 v[104:107], v[172:175], v[200:203], v[104:107]
	v_mfma_f32_16x16x32_bf16 v[100:103], v[180:183], v[200:203], v[100:103]
	v_mfma_f32_16x16x32_bf16 v[88:91], v[172:175], v[226:229], v[88:91]
	v_mfma_f32_16x16x32_bf16 v[84:87], v[180:183], v[226:229], v[84:87]
	v_mfma_f32_16x16x32_bf16 v[72:75], v[172:175], v[234:237], v[72:75]
	v_mfma_f32_16x16x32_bf16 v[68:71], v[180:183], v[234:237], v[68:71]
	s_barrier
	s_setprio 0
	s_add_i32 s26, s28, s46
	v_lshl_add_u64 v[154:155], v[154:155], 0, s[86:87]
	s_mov_b32 m0, s26
	ds_read_b128 v[188:191], v186 offset:49152
	ds_read_b128 v[192:195], v186 offset:50176
	ds_read_b128 v[196:199], v186 offset:51200
	ds_read_b128 v[200:203], v186 offset:52224
	ds_read_b128 v[222:225], v186 offset:53248
	ds_read_b128 v[226:229], v186 offset:54272
	ds_read_b128 v[230:233], v186 offset:55296
	ds_read_b128 v[234:237], v186 offset:56320
	global_load_lds_dwordx4 v[154:155], off
	s_add_i32 m0, s26, 0x2000
	s_add_u32 s24, s24, 0x100080
	v_lshl_add_u64 v[154:155], v[184:185], 0, s[86:87]
	s_addc_u32 s25, s25, 0
	s_add_i32 s26, s29, s46
	global_load_lds_dwordx4 v[154:155], off
	v_lshl_add_u64 v[154:155], s[24:25], 0, v[2:3]
	s_mov_b32 m0, s26
	s_nop 0
	global_load_lds_dwordx4 v[154:155], off
	v_lshl_add_u64 v[154:155], s[24:25], 0, v[132:133]
	s_add_i32 m0, s26, 0x2000
	s_nop 0
	global_load_lds_dwordx4 v[154:155], off
	v_lshl_add_u64 v[154:155], v[204:205], 0, s[86:87]
	s_mov_b32 m0, s76
	s_nop 0
	global_load_lds_dwordx4 v[154:155], off
	v_lshl_add_u64 v[154:155], v[238:239], 0, s[86:87]
	s_mov_b32 m0, s77
	s_nop 0
	global_load_lds_dwordx4 v[154:155], off
	s_waitcnt vmcnt(8)
	s_waitcnt lgkmcnt(0)
	s_setprio 1
	s_barrier
	v_mfma_f32_16x16x32_bf16 v[64:67], v[138:141], v[188:191], v[64:67]
	v_mfma_f32_16x16x32_bf16 v[60:63], v[146:149], v[188:191], v[60:63]
	v_mfma_f32_16x16x32_bf16 v[48:51], v[138:141], v[196:199], v[48:51]
	v_mfma_f32_16x16x32_bf16 v[44:47], v[146:149], v[196:199], v[44:47]
	v_mfma_f32_16x16x32_bf16 v[32:35], v[138:141], v[222:225], v[32:35]
	v_mfma_f32_16x16x32_bf16 v[28:31], v[146:149], v[222:225], v[28:31]
	v_mfma_f32_16x16x32_bf16 v[16:19], v[138:141], v[230:233], v[16:19]
	v_mfma_f32_16x16x32_bf16 v[12:15], v[146:149], v[230:233], v[12:15]
	v_mfma_f32_16x16x32_bf16 v[64:67], v[142:145], v[192:195], v[64:67]
	v_mfma_f32_16x16x32_bf16 v[60:63], v[150:153], v[192:195], v[60:63]
	v_mfma_f32_16x16x32_bf16 v[48:51], v[142:145], v[200:203], v[48:51]
	v_mfma_f32_16x16x32_bf16 v[44:47], v[150:153], v[200:203], v[44:47]
	v_mfma_f32_16x16x32_bf16 v[32:35], v[142:145], v[226:229], v[32:35]
	v_mfma_f32_16x16x32_bf16 v[28:31], v[150:153], v[226:229], v[28:31]
	v_mfma_f32_16x16x32_bf16 v[16:19], v[142:145], v[234:237], v[16:19]
	v_mfma_f32_16x16x32_bf16 v[12:15], v[150:153], v[234:237], v[12:15]
	v_mfma_f32_16x16x32_bf16 v[56:59], v[168:171], v[188:191], v[56:59]
	v_mfma_f32_16x16x32_bf16 v[52:55], v[176:179], v[188:191], v[52:55]
	v_mfma_f32_16x16x32_bf16 v[40:43], v[168:171], v[196:199], v[40:43]
	v_mfma_f32_16x16x32_bf16 v[36:39], v[176:179], v[196:199], v[36:39]
	v_mfma_f32_16x16x32_bf16 v[24:27], v[168:171], v[222:225], v[24:27]
	v_mfma_f32_16x16x32_bf16 v[20:23], v[176:179], v[222:225], v[20:23]
	v_mfma_f32_16x16x32_bf16 v[8:11], v[168:171], v[230:233], v[8:11]
	v_mfma_f32_16x16x32_bf16 v[4:7], v[176:179], v[230:233], v[4:7]
	v_mfma_f32_16x16x32_bf16 v[56:59], v[172:175], v[192:195], v[56:59]
	v_mfma_f32_16x16x32_bf16 v[52:55], v[180:183], v[192:195], v[52:55]
	v_mfma_f32_16x16x32_bf16 v[40:43], v[172:175], v[200:203], v[40:43]
	v_mfma_f32_16x16x32_bf16 v[36:39], v[180:183], v[200:203], v[36:39]
	v_mfma_f32_16x16x32_bf16 v[24:27], v[172:175], v[226:229], v[24:27]
	v_mfma_f32_16x16x32_bf16 v[20:23], v[180:183], v[226:229], v[20:23]
	v_mfma_f32_16x16x32_bf16 v[8:11], v[172:175], v[234:237], v[8:11]
	v_mfma_f32_16x16x32_bf16 v[4:7], v[180:183], v[234:237], v[4:7]
	s_barrier
	s_setprio 0
	s_add_i32 s58, s58, 2
	s_add_u32 s6, s6, 0x100
	s_addc_u32 s7, s7, 0
	s_add_u32 s21, s21, 0x100
	s_addc_u32 s13, s13, 0
	s_cmp_gt_u32 s58, 61
	s_cbranch_scc0 .LBB0_1202

.LBB0_1205:
	s_mov_b32 s101, 1
	s_lshl_b32 s6, s16, 8
	v_mov_b32_e32 v188, v157
	v_mov_b32_e32 v187, v1
	s_or_b32 s6, s6, s61
	s_lshl_b32 s17, s17, 8
	v_add_u32_e32 v189, s55, v187
	v_lshl_add_u32 v138, v188, 2, s6
	v_add_u32_e32 v142, s17, v189
	v_ashrrev_i32_e32 v139, 31, v138
	v_lshlrev_b64 v[144:145], 1, v[138:139]
	v_ashrrev_i32_e32 v143, 31, v142
	v_lshl_add_u64 v[140:141], s[8:9], 0, v[144:145]
	v_lshlrev_b64 v[148:149], 13, v[142:143]
	v_lshl_add_u64 v[146:147], v[140:141], 0, v[148:149]
	global_load_dwordx2 v[190:191], v[146:147], off
	global_load_dwordx2 v[192:193], v[146:147], off offset:32
	global_load_dwordx2 v[194:195], v[146:147], off offset:256
	global_load_dwordx2 v[196:197], v[146:147], off offset:288
	s_mov_b64 s[6:7], 0x40000
	v_lshl_add_u64 v[176:177], v[148:149], 0, s[94:95]
	v_lshl_add_u64 v[154:155], v[148:149], 0, s[6:7]
	s_mov_b64 s[6:7], 0x60000
	v_lshl_add_u64 v[146:147], v[148:149], 0, s[6:7]
	v_lshl_add_u64 v[148:149], s[8:9], 0, v[148:149]
	v_lshl_add_u64 v[150:151], v[140:141], 0, v[176:177]
	v_lshl_add_u64 v[152:153], v[140:141], 0, v[154:155]
	v_lshl_add_u64 v[198:199], v[140:141], 0, v[146:147]
	v_lshl_add_u64 v[200:201], v[148:149], 0, v[144:145]
	global_load_dwordx2 v[184:185], v[150:151], off
	global_load_dwordx2 v[182:183], v[150:151], off offset:32
	global_load_dwordx2 v[180:181], v[150:151], off offset:256
	global_load_dwordx2 v[178:179], v[150:151], off offset:288
	global_load_dwordx2 v[174:175], v[152:153], off
	global_load_dwordx2 v[172:173], v[152:153], off offset:32
	global_load_dwordx2 v[170:171], v[152:153], off offset:256
	global_load_dwordx2 v[168:169], v[152:153], off offset:288
	s_nop 0
	global_load_dwordx2 v[152:153], v[198:199], off
	global_load_dwordx2 v[150:151], v[198:199], off offset:32
	global_load_dwordx2 v[148:149], v[198:199], off offset:256
	global_load_dwordx2 v[144:145], v[198:199], off offset:288
	v_cmp_eq_u32_e32 vcc, 0, v188
	s_waitcnt vmcnt(0)
	v_lshlrev_b32_e32 v198, 16, v190
	v_and_b32_e32 v190, 0xffff0000, v190
	v_lshlrev_b32_e32 v199, 16, v191
	v_and_b32_e32 v191, 0xffff0000, v191
	v_lshlrev_b32_e32 v202, 16, v192
	v_and_b32_e32 v192, 0xffff0000, v192
	v_lshlrev_b32_e32 v203, 16, v193
	v_and_b32_e32 v193, 0xffff0000, v193
	v_lshlrev_b32_e32 v204, 16, v194
	v_and_b32_e32 v194, 0xffff0000, v194
	v_lshlrev_b32_e32 v205, 16, v195
	v_and_b32_e32 v195, 0xffff0000, v195
	v_lshlrev_b32_e32 v222, 16, v196
	v_and_b32_e32 v196, 0xffff0000, v196
	v_add_f32_e32 v129, v129, v190
	v_add_f32_e32 v131, v131, v191
	v_add_f32_e32 v125, v125, v192
	v_add_f32_e32 v127, v127, v193
	v_lshlrev_b32_e32 v223, 16, v197
	v_and_b32_e32 v197, 0xffff0000, v197
	v_add_f32_e32 v128, v128, v198
	v_add_f32_e32 v130, v130, v199
	v_add_f32_e32 v124, v124, v202
	v_add_f32_e32 v126, v126, v203
	v_add_f32_e32 v121, v121, v194
	v_add_f32_e32 v123, v123, v195
	v_add_f32_e32 v190, v116, v222
	v_add_f32_e32 v191, v117, v196
	v_mul_f32_e32 v194, v129, v129
	v_mul_f32_e32 v195, v131, v131
	v_cvt_pk_bf16_f32 v116, v128, v129
	v_cvt_pk_bf16_f32 v117, v130, v131
	v_mul_f32_e32 v129, v125, v125
	v_mul_f32_e32 v131, v127, v127
	v_add_f32_e32 v120, v120, v204
	v_add_f32_e32 v122, v122, v205
	v_add_f32_e32 v193, v119, v197
	v_mul_f32_e32 v196, v121, v121
	v_mul_f32_e32 v197, v123, v123
	v_fmac_f32_e32 v194, v128, v128
	v_fmac_f32_e32 v195, v130, v130
	v_fmac_f32_e32 v129, v124, v124
	v_fmac_f32_e32 v131, v126, v126
	global_store_dwordx2 v[200:201], v[116:117], off
	v_fmac_f32_e32 v196, v120, v120
	v_fmac_f32_e32 v197, v122, v122
	v_add_f32_e32 v116, v194, v195
	v_add_f32_e32 v117, v129, v131
	v_add_f32_e32 v192, v118, v223
	v_cvt_pk_bf16_f32 v118, v124, v125
	v_add_f32_e32 v124, v196, v197
	v_add_f32_e32 v116, v116, v117
	v_add_f32_e32 v116, v116, v124
	v_mul_f32_e32 v117, v191, v191
	v_mul_f32_e32 v124, v193, v193
	v_fmac_f32_e32 v117, v190, v190
	v_fmac_f32_e32 v124, v192, v192
	v_add_f32_e32 v117, v117, v124
	v_and_b32_e32 v124, 64, v212
	v_add_f32_e32 v116, v116, v117
	v_xor_b32_e32 v117, 16, v212
	v_add_u32_e32 v124, 64, v124
	v_cmp_lt_i32_e64 s[6:7], v117, v124
	v_cvt_pk_bf16_f32 v119, v126, v127
	global_store_dwordx2 v[200:201], v[118:119], off offset:32
	v_cvt_pk_bf16_f32 v118, v120, v121
	v_cvt_pk_bf16_f32 v119, v122, v123
	global_store_dwordx2 v[200:201], v[118:119], off offset:256
	v_cndmask_b32_e64 v117, v212, v117, s[6:7]
	v_lshlrev_b32_e32 v117, 2, v117
	ds_bpermute_b32 v125, v117, v116
	v_cvt_pk_bf16_f32 v122, v190, v191
	v_cvt_pk_bf16_f32 v123, v192, v193
	global_store_dwordx2 v[200:201], v[122:123], off offset:288
	s_waitcnt lgkmcnt(0)
	v_add_f32_e32 v119, v116, v125
	v_xor_b32_e32 v116, 32, v212
	v_cmp_lt_i32_e64 s[6:7], v116, v124
	s_nop 1
	v_cndmask_b32_e64 v116, v212, v116, s[6:7]
	v_lshlrev_b32_e32 v118, 2, v116
	ds_bpermute_b32 v120, v118, v119
	v_lshl_add_u32 v116, v189, 4, s88
	s_and_saveexec_b64 s[6:7], vcc
	s_movk_i32 s71, 0x2000
	s_mov_b32 s92, 0xc2fc0000
	s_cbranch_execz .LBB0_1207
	s_waitcnt lgkmcnt(0)
	v_add_f32_e32 v119, v119, v120
	ds_write_b32 v116, v119

	.amdhsa_kernel _Z9hymba_fwd4Args
		.amdhsa_group_segment_fixed_size 0
		.amdhsa_private_segment_fixed_size 0
		.amdhsa_kernarg_size 432
		.amdhsa_user_sgpr_count 2
		.amdhsa_user_sgpr_dispatch_ptr 0
		.amdhsa_user_sgpr_queue_ptr 0
		.amdhsa_user_sgpr_kernarg_segment_ptr 1
		.amdhsa_user_sgpr_dispatch_id 0
		.amdhsa_user_sgpr_kernarg_preload_length 0
		.amdhsa_user_sgpr_kernarg_preload_offset 0
		.amdhsa_user_sgpr_private_segment_size 0
		.amdhsa_uses_dynamic_stack 0
		.amdhsa_enable_private_segment 0
		.amdhsa_system_sgpr_workgroup_id_x 1
		.amdhsa_system_sgpr_workgroup_id_y 0
		.amdhsa_system_sgpr_workgroup_id_z 0
		.amdhsa_system_sgpr_workgroup_info 0
		.amdhsa_system_vgpr_workitem_id 0
		.amdhsa_next_free_vgpr 255
		.amdhsa_next_free_sgpr 102
		.amdhsa_accum_offset 256
		.amdhsa_reserve_vcc 1
		.amdhsa_float_round_mode_32 0
		.amdhsa_float_round_mode_16_64 0
		.amdhsa_float_denorm_mode_32 3
		.amdhsa_float_denorm_mode_16_64 3
		.amdhsa_dx10_clamp 1
		.amdhsa_ieee_mode 1
		.amdhsa_fp16_overflow 0
		.amdhsa_tg_split 0
		.amdhsa_exception_fp_ieee_invalid_op 0
		.amdhsa_exception_fp_denorm_src 0
		.amdhsa_exception_fp_ieee_div_zero 0
		.amdhsa_exception_fp_ieee_overflow 0
		.amdhsa_exception_fp_ieee_underflow 0
		.amdhsa_exception_fp_ieee_inexact 0
		.amdhsa_exception_int_div_zero 0
	.end_amdhsa_kernel

amdhsa.kernels:
  - .agpr_count:     0
    .args:
      - .offset:         0
        .size:           176
        .value_kind:     by_value
      - .offset:         176
        .size:           4
        .value_kind:     hidden_block_count_x
      - .offset:         180
        .size:           4
        .value_kind:     hidden_block_count_y
      - .offset:         184
        .size:           4
        .value_kind:     hidden_block_count_z
      - .offset:         188
        .size:           2
        .value_kind:     hidden_group_size_x
      - .offset:         190
        .size:           2
        .value_kind:     hidden_group_size_y
      - .offset:         192
        .size:           2
        .value_kind:     hidden_group_size_z
      - .offset:         194
        .size:           2
        .value_kind:     hidden_remainder_x
      - .offset:         196
        .size:           2
        .value_kind:     hidden_remainder_y
      - .offset:         198
        .size:           2
        .value_kind:     hidden_remainder_z
      - .offset:         216
        .size:           8
        .value_kind:     hidden_global_offset_x
      - .offset:         224
        .size:           8
        .value_kind:     hidden_global_offset_y
      - .offset:         232
        .size:           8
        .value_kind:     hidden_global_offset_z
      - .offset:         240
        .size:           2
        .value_kind:     hidden_grid_dims
      - .offset:         296
        .size:           4
        .value_kind:     hidden_dynamic_lds_size
    .group_segment_fixed_size: 0
    .kernarg_segment_align: 8
    .kernarg_segment_size: 432
    .language:       OpenCL C
    .language_version:
      - 2
      - 0
    .max_flat_workgroup_size: 512
    .name:           _Z9hymba_fwd4Args
    .private_segment_fixed_size: 0
    .sgpr_count:     108
    .sgpr_spill_count: 133
    .symbol:         _Z9hymba_fwd4Args.kd
    .uniform_work_group_size: 1
    .uses_dynamic_stack: false
    .vgpr_count:     255
    .vgpr_spill_count: 0
    .wavefront_size: 64
